# kvloc (phase 2): transposed LDS fragment reads software-pipelined two MFMA groups ahead (3 B temp sets in free VGPRs)
# speedup vs baseline: 1.0002x; 1.0002x over previous
.LBB0_408:
	s_waitcnt lgkmcnt(0)
	s_barrier
	ds_read_b64_tr_b16 v[102:103], v141 offset:2048
	ds_read_b64_tr_b16 v[104:105], v141 offset:3136
	ds_read_b64_tr_b16 v[170:171], v123 offset:19456
	ds_read_b64_tr_b16 v[172:173], v123 offset:21696
	ds_read_b64_tr_b16 v[174:175], v123 offset:19488
	ds_read_b64_tr_b16 v[176:177], v123 offset:21728
	ds_read_b64_tr_b16 v[178:179], v123 offset:19520
	ds_read_b64_tr_b16 v[180:181], v123 offset:21760
	ds_read_b64_tr_b16 v[182:183], v123 offset:19552
	ds_read_b64_tr_b16 v[184:185], v123 offset:21792
	ds_read_b64_tr_b16 v[194:195], v123 offset:19584
	ds_read_b64_tr_b16 v[196:197], v123 offset:21824
	ds_read_b64_tr_b16 v[198:199], v123 offset:19616
	ds_read_b64_tr_b16 v[200:201], v123 offset:21856
	s_waitcnt lgkmcnt(8)
	v_mfma_f32_16x16x32_bf16 v[98:101], v[102:105], v[170:173], v[98:101]
	v_mfma_f32_16x16x32_bf16 v[94:97], v[102:105], v[174:177], v[94:97]
	ds_read_b64_tr_b16 v[170:171], v123 offset:19648
	ds_read_b64_tr_b16 v[172:173], v123 offset:21888
	ds_read_b64_tr_b16 v[174:175], v123 offset:19680
	ds_read_b64_tr_b16 v[176:177], v123 offset:21920
	s_waitcnt lgkmcnt(8)
	v_mfma_f32_16x16x32_bf16 v[90:93], v[102:105], v[178:181], v[90:93]
	v_mfma_f32_16x16x32_bf16 v[86:89], v[102:105], v[182:185], v[86:89]
	ds_read_b64_tr_b16 v[178:179], v123 offset:19712
	ds_read_b64_tr_b16 v[180:181], v123 offset:21952
	ds_read_b64_tr_b16 v[182:183], v123 offset:19744
	ds_read_b64_tr_b16 v[184:185], v123 offset:21984
	s_waitcnt lgkmcnt(8)
	v_mfma_f32_16x16x32_bf16 v[82:85], v[102:105], v[194:197], v[82:85]
	v_mfma_f32_16x16x32_bf16 v[78:81], v[102:105], v[198:201], v[78:81]
	ds_read_b64_tr_b16 v[194:195], v123 offset:19776
	ds_read_b64_tr_b16 v[196:197], v123 offset:22016
	ds_read_b64_tr_b16 v[198:199], v123 offset:19808
	ds_read_b64_tr_b16 v[200:201], v123 offset:22048
	s_waitcnt lgkmcnt(8)
	v_mfma_f32_16x16x32_bf16 v[74:77], v[102:105], v[170:173], v[74:77]
	v_mfma_f32_16x16x32_bf16 v[70:73], v[102:105], v[174:177], v[70:73]
	ds_read_b64_tr_b16 v[170:171], v123 offset:19840
	ds_read_b64_tr_b16 v[172:173], v123 offset:22080
	ds_read_b64_tr_b16 v[174:175], v123 offset:19872
	ds_read_b64_tr_b16 v[176:177], v123 offset:22112
	s_waitcnt lgkmcnt(8)
	v_mfma_f32_16x16x32_bf16 v[66:69], v[102:105], v[178:181], v[66:69]
	v_mfma_f32_16x16x32_bf16 v[62:65], v[102:105], v[182:185], v[62:65]
	ds_read_b64_tr_b16 v[178:179], v123 offset:19904
	ds_read_b64_tr_b16 v[180:181], v123 offset:22144
	ds_read_b64_tr_b16 v[182:183], v123 offset:19936
	ds_read_b64_tr_b16 v[184:185], v123 offset:22176
	s_waitcnt lgkmcnt(8)
	v_mfma_f32_16x16x32_bf16 v[58:61], v[102:105], v[194:197], v[58:61]
	v_mfma_f32_16x16x32_bf16 v[54:57], v[102:105], v[198:201], v[54:57]
	ds_read_b64_tr_b16 v[194:195], v123 offset:19968
	ds_read_b64_tr_b16 v[196:197], v123 offset:22208
	s_waitcnt lgkmcnt(6)
	v_mfma_f32_16x16x32_bf16 v[46:49], v[102:105], v[170:173], v[46:49]
	v_mfma_f32_16x16x32_bf16 v[42:45], v[102:105], v[174:177], v[42:45]
	ds_read_b64_tr_b16 v[202:203], v141 offset:10752
	ds_read_b64_tr_b16 v[204:205], v141 offset:11840
	ds_read_b64_tr_b16 v[170:171], v123 offset:37376
	ds_read_b64_tr_b16 v[172:173], v123 offset:39616
	ds_read_b64_tr_b16 v[174:175], v123 offset:37408
	ds_read_b64_tr_b16 v[176:177], v123 offset:39648
	s_waitcnt lgkmcnt(8)
	v_mfma_f32_16x16x32_bf16 v[38:41], v[102:105], v[178:181], v[38:41]
	v_mfma_f32_16x16x32_bf16 v[34:37], v[102:105], v[182:185], v[34:37]
	ds_read_b64_tr_b16 v[178:179], v123 offset:37440
	ds_read_b64_tr_b16 v[180:181], v123 offset:39680
	ds_read_b64_tr_b16 v[182:183], v123 offset:37472
	ds_read_b64_tr_b16 v[184:185], v123 offset:39712
	s_waitcnt lgkmcnt(10)
	v_mfma_f32_16x16x32_bf16 v[50:53], v[102:105], v[194:197], v[50:53]
	ds_read_b64_tr_b16 v[194:195], v123 offset:37504
	ds_read_b64_tr_b16 v[196:197], v123 offset:39744
	ds_read_b64_tr_b16 v[198:199], v123 offset:37536
	ds_read_b64_tr_b16 v[200:201], v123 offset:39776
	s_waitcnt lgkmcnt(8)
	v_mfma_f32_16x16x32_bf16 v[98:101], v[202:205], v[170:173], v[98:101]
	v_mfma_f32_16x16x32_bf16 v[94:97], v[202:205], v[174:177], v[94:97]
	ds_read_b64_tr_b16 v[170:171], v123 offset:37568
	ds_read_b64_tr_b16 v[172:173], v123 offset:39808
	ds_read_b64_tr_b16 v[174:175], v123 offset:37600
	ds_read_b64_tr_b16 v[176:177], v123 offset:39840
	s_waitcnt lgkmcnt(8)
	v_mfma_f32_16x16x32_bf16 v[90:93], v[202:205], v[178:181], v[90:93]
	v_mfma_f32_16x16x32_bf16 v[86:89], v[202:205], v[182:185], v[86:89]
	ds_read_b64_tr_b16 v[178:179], v123 offset:37632
	ds_read_b64_tr_b16 v[180:181], v123 offset:39872
	ds_read_b64_tr_b16 v[182:183], v123 offset:37664
	ds_read_b64_tr_b16 v[184:185], v123 offset:39904
	s_waitcnt lgkmcnt(8)
	v_mfma_f32_16x16x32_bf16 v[82:85], v[202:205], v[194:197], v[82:85]
	v_mfma_f32_16x16x32_bf16 v[78:81], v[202:205], v[198:201], v[78:81]
	ds_read_b64_tr_b16 v[194:195], v123 offset:37696
	ds_read_b64_tr_b16 v[196:197], v123 offset:39936
	ds_read_b64_tr_b16 v[198:199], v123 offset:37728
	ds_read_b64_tr_b16 v[200:201], v123 offset:39968
	s_waitcnt lgkmcnt(8)
	v_mfma_f32_16x16x32_bf16 v[74:77], v[202:205], v[170:173], v[74:77]
	v_mfma_f32_16x16x32_bf16 v[70:73], v[202:205], v[174:177], v[70:73]
	ds_read_b64_tr_b16 v[170:171], v123 offset:37760
	ds_read_b64_tr_b16 v[172:173], v123 offset:40000
	ds_read_b64_tr_b16 v[174:175], v123 offset:37792
	ds_read_b64_tr_b16 v[176:177], v123 offset:40032
	s_waitcnt lgkmcnt(8)
	v_mfma_f32_16x16x32_bf16 v[66:69], v[202:205], v[178:181], v[66:69]
	v_mfma_f32_16x16x32_bf16 v[62:65], v[202:205], v[182:185], v[62:65]
	ds_read_b64_tr_b16 v[178:179], v123 offset:37824
	ds_read_b64_tr_b16 v[180:181], v123 offset:40064
	ds_read_b64_tr_b16 v[182:183], v123 offset:37856
	ds_read_b64_tr_b16 v[184:185], v123 offset:40096
	s_waitcnt lgkmcnt(8)
	v_mfma_f32_16x16x32_bf16 v[58:61], v[202:205], v[194:197], v[58:61]
	v_mfma_f32_16x16x32_bf16 v[54:57], v[202:205], v[198:201], v[54:57]
	ds_read_b64_tr_b16 v[194:195], v123 offset:37888
	ds_read_b64_tr_b16 v[196:197], v123 offset:40128
	s_waitcnt lgkmcnt(6)
	v_mfma_f32_16x16x32_bf16 v[46:49], v[202:205], v[170:173], v[46:49]
	v_mfma_f32_16x16x32_bf16 v[42:45], v[202:205], v[174:177], v[42:45]
	s_waitcnt lgkmcnt(2)
	v_mfma_f32_16x16x32_bf16 v[38:41], v[202:205], v[178:181], v[38:41]
	v_mfma_f32_16x16x32_bf16 v[34:37], v[202:205], v[182:185], v[34:37]
	s_waitcnt lgkmcnt(0)
	s_add_i32 s62, s62, 64
	s_add_i32 s64, s64, 1
	v_add_u32_e32 v168, 0x100, v168
	s_cmp_eq_u32 s40, s62
	v_mfma_f32_16x16x32_bf16 v[50:53], v[202:205], v[194:197], v[50:53]
	v_add_u32_e32 v167, 0x100, v167
	s_cbranch_scc1 .LBB0_424
